# select v2: mlstm_pre half-items on all waves, final pass without tie logic when all ties are taken
# baseline (speedup 1.0000x reference)
.LBB0_1198:
	s_cmp_lt_i32 s92, 7
	s_cselect_b64 s[0:1], -1, 0
	s_cmp_gt_i32 s93, 6
	s_cselect_b64 s[2:3], -1, 0
	s_and_b64 s[0:1], s[0:1], s[2:3]
	s_andn2_b64 vcc, exec, s[0:1]
	s_cbranch_vccnz .LBB0_1918
	v_mov_b32_e32 v2, v0
	s_nop 0
	v_readfirstlane_b32 s0, v2
	s_ashr_i32 s12, s0, 6
	s_lshl_b32 s0, s90, 3
	s_add_i32 s3, s12, s0
	s_cmpk_eq_i32 s84, 0x100
	s_cselect_b32 s98, 1, 0
	s_and_b32 s101, s3, s98
	s_xor_b32 s100, s101, s98
	s_lshl_b32 s100, s100, 1
	s_add_i32 s100, s100, 1
	s_sub_i32 s101, 4, s101
	s_lshl_b32 s99, 0x400, s98
	s_cmp_lt_i32 s3, s99
	s_waitcnt vmcnt(0)
	v_and_b32_e32 v50, 63, v2
	s_cbranch_scc1 .LBB0_1201
	s_lshl_b32 s2, s12, 14
	s_lshl_b32 s35, s84, 3
	v_mov_b32_e32 v51, 0
	s_cbranch_execz .LBB0_1202
	s_branch .LBB0_1220
.LBB0_1201:
.LBB0_1202:
	s_add_u32 s0, s30, 0xa800000
	s_addc_u32 s1, s31, 0
	s_add_u32 s4, s30, 0xa840000
	s_addc_u32 s5, s31, 0
	s_add_u32 s22, s30, 0x6a400000
	s_addc_u32 s23, s31, 0
	s_add_u32 s6, s30, 0x6ac00000
	s_addc_u32 s7, s31, 0
	s_add_u32 s8, s30, 0x6ac40000
	s_addc_u32 s9, s31, 0
	s_add_u32 s10, s30, 0x6ac80000
	v_mov_b32_e32 v39, 0
	v_and_b32_e32 v38, 48, v50
	s_addc_u32 s11, s31, 0
	s_lshl_b32 s2, s12, 14
	v_lshl_add_u64 v[4:5], s[30:31], 0, v[38:39]
	s_mov_b64 s[14:15], 0xb100000
	v_lshrrev_b32_e32 v3, 2, v50
	v_and_b32_e32 v38, 48, v2
	s_add_i32 s33, s2, 0
	v_and_b32_e32 v1, 15, v2
	v_lshl_add_u64 v[40:41], v[4:5], 0, s[14:15]
	v_and_b32_e32 v53, 12, v3
	v_lshl_add_u64 v[2:3], s[30:31], 0, v[38:39]
	s_mov_b64 s[14:15], 0xd100100
	s_lshl_b32 s13, s90, 9
	s_lshl_b32 s12, s12, 6
	v_mov_b32_e32 v51, v39
	v_lshl_add_u32 v52, v50, 2, s33
	s_lshl_b32 s35, s84, 3
	v_lshl_add_u32 v54, v1, 2, s33
	v_lshl_add_u64 v[42:43], v[2:3], 0, s[14:15]
	v_lshlrev_b32_e32 v55, 11, v1
	s_add_i32 s34, s13, s12
	s_lshr_b32 s34, s34, s98
	s_andn2_b32 s34, s34, 63
	s_lshl_b32 s36, s84, 9
	s_mov_b64 s[12:13], 0x10000
	s_lshr_b32 s14, s3, s98
	s_branch .LBB0_1204

.LBB0_1204:
	s_lshl_b32 s15, s14, 6
	s_and_b32 s37, s15, 0x1fc0
	s_ashr_i32 s20, s14, 7
	s_waitcnt vmcnt(11)
	v_or_b32_e32 v2, s37, v50
	v_lshlrev_b32_e32 v2, 3, v2
	v_mov_b32_e32 v3, v39
	s_ashr_i32 s21, s20, 31
	v_lshl_add_u64 v[2:3], v[2:3], 0, s[20:21]
	v_lshlrev_b64 v[2:3], 2, v[2:3]
	v_lshl_add_u64 v[4:5], s[4:5], 0, v[2:3]
	global_load_dword v8, v[4:5], off
	v_lshl_add_u64 v[2:3], s[0:1], 0, v[2:3]
	global_load_dword v9, v[2:3], off
	s_lshl_b32 s18, s34, 12
	s_waitcnt vmcnt(11)
	v_mov_b32_e32 v10, v39
	s_and_b32 s38, s18, 0x1fc0000
	v_mov_b32_e32 v11, v39
	s_ashr_i32 s15, s14, 31
	v_lshl_or_b32 v38, v55, 1, s38
	s_lshl_b64 s[38:39], s[20:21], 13
	s_lshl_b64 s[18:19], s[14:15], 13
	s_or_b32 s15, s38, s37
	v_mov_b32_e32 v3, s39
	v_or_b32_e32 v2, s15, v50
	v_mov_b32_e32 v12, 0xff800000
	v_lshlrev_b64 v[2:3], 2, v[2:3]
	v_lshl_add_u64 v[4:5], s[6:7], 0, v[2:3]
	v_mov_b32_e32 v13, 0xff800000
	s_waitcnt vmcnt(10)
	v_mov_b32_e32 v14, 0xff800000
	v_mov_b32_e32 v15, 0xff800000
	v_mov_b32_e32 v16, 0xff800000
	v_mov_b32_e32 v17, 0xff800000
	s_add_u32 s18, s22, s18
	v_lshl_add_u64 v[6:7], s[8:9], 0, v[2:3]
	v_lshl_add_u64 v[2:3], s[10:11], 0, v[2:3]
	s_addc_u32 s19, s23, s19
	s_lshl_b32 s20, s20, 8
	s_ashr_i32 s21, s20, 31
	s_lshl_b64 s[20:21], s[20:21], 1
	s_waitcnt vmcnt(9)
	v_or_b32_e32 v18, s37, v1
	v_lshl_add_u64 v[44:45], v[40:41], 0, s[20:21]
	v_lshlrev_b32_e32 v56, 11, v18
	s_and_b32 s15, s3, s98
	s_waitcnt vmcnt(1)
	v_add_f32_dpp v8, v8, v8 row_shr:1 row_mask:0xf bank_mask:0xf bound_ctrl:1
	s_nop 1
	v_add_f32_dpp v8, v8, v8 row_shr:2 row_mask:0xf bank_mask:0xf bound_ctrl:1
	s_nop 1
	v_add_f32_dpp v8, v8, v8 row_shr:4 row_mask:0xf bank_mask:0xf bound_ctrl:1
	s_nop 1
	v_add_f32_dpp v8, v8, v8 row_shr:8 row_mask:0xf bank_mask:0xf bound_ctrl:1
	s_nop 1
	v_mov_b32_dpp v10, v8 row_bcast:15 row_mask:0xa bank_mask:0xf
	v_add_f32_e32 v8, v8, v10
	s_nop 1
	v_mov_b32_dpp v11, v8 row_bcast:31 row_mask:0xc bank_mask:0xf
	v_add_f32_e32 v8, v8, v11
	s_waitcnt vmcnt(0)
	v_sub_f32_e32 v9, v9, v8
	global_store_dword v[4:5], v9, off
	global_store_dword v[6:7], v8, off
	v_mov_b32_dpp v12, v9 row_shr:1 row_mask:0xf bank_mask:0xf
	v_max_f32_e32 v4, v12, v12
	v_max_f32_e32 v4, v9, v4
	s_nop 1
	v_mov_b32_dpp v13, v4 row_shr:2 row_mask:0xf bank_mask:0xf
	v_max_f32_e32 v5, v13, v13
	v_max_f32_e32 v4, v4, v5
	s_nop 1
	v_mov_b32_dpp v14, v4 row_shr:4 row_mask:0xf bank_mask:0xf
	v_max_f32_e32 v5, v14, v14
	v_max_f32_e32 v4, v4, v5
	s_nop 1
	v_mov_b32_dpp v15, v4 row_shr:8 row_mask:0xf bank_mask:0xf
	v_max_f32_e32 v5, v15, v15
	v_max_f32_e32 v4, v4, v5
	s_nop 1
	v_mov_b32_dpp v16, v4 row_bcast:15 row_mask:0xa bank_mask:0xf
	v_max_f32_e32 v5, v16, v16
	v_max_f32_e32 v4, v4, v5
	s_nop 1
	v_mov_b32_dpp v17, v4 row_bcast:31 row_mask:0xc bank_mask:0xf
	v_max_f32_e32 v5, v17, v17
	v_max_f32_e32 v4, v4, v5
	global_store_dword v[2:3], v4, off
	ds_write2st64_b32 v52, v9, v4 offset1:1
	s_waitcnt lgkmcnt(0)
	v_lshl_add_u64 v[2:3], s[20:21], 0, v[38:39]
	v_lshl_add_u64 v[46:47], v[42:43], 0, v[2:3]
	s_branch .LBB0_1206
.LBB0_1205:
	s_add_i32 s15, s15, s100
	s_cmp_ge_u32 s15, s101
	s_cbranch_scc1 .LBB0_1203

.LBB0_1234:
	s_or_b64 exec, exec, s[4:5]
	s_lshl_b64 s[4:5], s[38:39], 10
	s_add_u32 s40, s48, s4
	s_addc_u32 s41, s49, s5
	s_cmpk_gt_i32 s38, 0xff
	s_mov_b64 s[4:5], -1
	s_cbranch_scc0 .LBB0_1866
	s_add_i32 s2, s38, 1
	s_lshl_b64 s[42:43], s[38:39], 15
	s_add_u32 s42, s46, s42
	s_addc_u32 s43, s47, s43
	v_lshlrev_b32_e32 v58, 4, v50
	v_mov_b32_e32 v150, 0
	v_mov_b32_e32 v151, 0
	v_mov_b32_e32 v152, 0
	v_mov_b32_e32 v153, 0
	v_add_u32_e32 v64, s52, v58
	s_movk_i32 s15, 0x100
	v_and_b32_e32 v146, 1, v50
	v_mul_u32_u24_e32 v147, 8, v146
	v_sub_u32_e32 v147, 4, v147
	v_mul_u32_u24_e32 v146, 0x3ffc, v146
	v_add_u32_e32 v146, s52, v146
	s_mov_b64 s[8:9], s[42:43]
	global_load_dwordx4 v[2:5], v58, s[8:9]
	global_load_dwordx4 v[6:9], v58, s[8:9] offset:1024
	global_load_dwordx4 v[10:13], v58, s[8:9] offset:2048
	global_load_dwordx4 v[14:17], v58, s[8:9] offset:3072
	ds_write_b128 v64, v[150:153]
	ds_write_b128 v64, v[150:153] offset:1024
	ds_write_b128 v64, v[150:153] offset:2048
	ds_write_b128 v64, v[150:153] offset:3072
	ds_write_b128 v64, v[150:153] offset:4096
	ds_write_b128 v64, v[150:153] offset:5120
	ds_write_b128 v64, v[150:153] offset:6144
	ds_write_b128 v64, v[150:153] offset:7168
	s_mov_b32 s16, 0
	s_waitcnt vmcnt(0)

.Lsel_p3_done:
	s_waitcnt lgkmcnt(0)
	v_lshl_add_u32 v34, v50, 6, s52
	ds_read_b128 v[2:5], v34
	ds_read_b128 v[6:9], v34 offset:16
	ds_read_b128 v[10:13], v34 offset:32
	ds_read_b128 v[14:17], v34 offset:48
	s_waitcnt lgkmcnt(0)
	v_add_u32_e32 v35, v2, v3
	v_add3_u32 v35, v35, v4, v5
	v_add3_u32 v35, v35, v6, v7
	v_add3_u32 v35, v35, v8, v9
	v_add3_u32 v35, v35, v10, v11
	v_add3_u32 v35, v35, v12, v13
	v_add3_u32 v35, v35, v14, v15
	v_add3_u32 v35, v35, v16, v17
	v_mov_b32_e32 v36, v35
	s_nop 1
	v_add_u32_dpp v36, v36, v36 row_shr:1 row_mask:0xf bank_mask:0xf bound_ctrl:1
	s_nop 1
	v_add_u32_dpp v36, v36, v36 row_shr:2 row_mask:0xf bank_mask:0xf bound_ctrl:1
	s_nop 1
	v_add_u32_dpp v36, v36, v36 row_shr:4 row_mask:0xf bank_mask:0xf bound_ctrl:1
	s_nop 1
	v_add_u32_dpp v36, v36, v36 row_shr:8 row_mask:0xf bank_mask:0xf bound_ctrl:1
	s_nop 1
	v_add_u32_dpp v36, v36, v36 row_bcast:15 row_mask:0xa bank_mask:0xf
	s_nop 1
	v_add_u32_dpp v36, v36, v36 row_bcast:31 row_mask:0xc bank_mask:0xf
	s_nop 0
	v_readlane_b32 s4, v36, 63
	s_nop 1
	v_sub_u32_e32 v37, s4, v36
	v_add_u32_e32 v38, v37, v35
	v_cmp_gt_u32_e32 vcc, s15, v37
	v_cmp_le_u32_e64 s[4:5], s15, v38
	s_and_b64 s[4:5], vcc, s[4:5]
	s_ff1_i32_b64 s6, s[4:5]
	v_readlane_b32 s7, v37, s6
	s_lshl_b32 s10, s6, 6
	s_add_i32 s10, s10, s52
	s_addk_i32 s10, 60
	v_and_b32_e32 v39, 15, v50
	v_lshlrev_b32_e32 v39, 2, v39
	v_sub_u32_e32 v39, s10, v39
	ds_read_b32 v40, v39
	v_cmp_gt_u32_e32 vcc, 16, v50
	s_waitcnt lgkmcnt(0)
	s_nop 1
	v_cndmask_b32_e32 v40, 0, v40, vcc
	v_mov_b32_e32 v41, v40
	s_nop 1
	v_add_u32_dpp v41, v41, v41 row_shr:1 row_mask:0xf bank_mask:0xf bound_ctrl:1
	s_nop 1
	v_add_u32_dpp v41, v41, v41 row_shr:2 row_mask:0xf bank_mask:0xf bound_ctrl:1
	s_nop 1
	v_add_u32_dpp v41, v41, v41 row_shr:4 row_mask:0xf bank_mask:0xf bound_ctrl:1
	s_nop 1
	v_add_u32_dpp v41, v41, v41 row_shr:8 row_mask:0xf bank_mask:0xf bound_ctrl:1
	s_nop 1
	v_add_u32_dpp v41, v41, v41 row_bcast:15 row_mask:0xa bank_mask:0xf
	s_nop 1
	v_add_u32_dpp v41, v41, v41 row_bcast:31 row_mask:0xc bank_mask:0xf
	s_nop 0
	v_sub_u32_e32 v42, v41, v40
	v_add_u32_e32 v42, s7, v42
	v_add_u32_e32 v43, v42, v40
	v_cmp_gt_u32_e32 vcc, s15, v42
	v_cmp_le_u32_e64 s[4:5], s15, v43
	s_and_b64 s[4:5], vcc, s[4:5]
	s_ff1_i32_b64 s11, s[4:5]
	v_readlane_b32 s29, v40, s11
	v_readlane_b32 s5, v42, s11
	s_lshl_b32 s28, s6, 4
	s_sub_i32 s4, 15, s11
	s_add_i32 s28, s28, s4
	s_sub_i32 s15, s15, s5
	s_lshl_b32 s17, s17, 10
	s_or_b32 s17, s17, s28
	s_mov_b32 s26, 0
	s_mov_b32 s27, 0
	s_cmp_eq_u32 s15, s29
	s_cbranch_scc1 .Lsel_simple
	s_mov_b64 s[8:9], s[42:43]
	global_load_dwordx4 v[2:5], v58, s[8:9]
	global_load_dwordx4 v[6:9], v58, s[8:9] offset:1024
	global_load_dwordx4 v[10:13], v58, s[8:9] offset:2048
	global_load_dwordx4 v[14:17], v58, s[8:9] offset:3072
	s_mov_b32 s16, 0
	s_waitcnt vmcnt(0)

.Lsel_simple:
	s_mov_b64 s[8:9], s[42:43]
	global_load_dwordx4 v[2:5], v58, s[8:9]
	global_load_dwordx4 v[6:9], v58, s[8:9] offset:1024
	global_load_dwordx4 v[10:13], v58, s[8:9] offset:2048
	global_load_dwordx4 v[14:17], v58, s[8:9] offset:3072
	s_mov_b32 s16, 0
	s_waitcnt vmcnt(0)

.Lsel_fs_nold:
	s_cmp_le_i32 s36, s2
	s_cbranch_scc0 .Lsel_fs_tail
	v_add_u32_e32 v145, s16, v56
	v_ashrrev_i32_e32 v34, 31, v18
	v_or_b32_e32 v34, 0x80000000, v34
	v_xor_b32_e32 v34, v18, v34
	v_ashrrev_i32_e32 v35, 31, v19
	v_or_b32_e32 v35, 0x80000000, v35
	v_xor_b32_e32 v35, v19, v35
	v_ashrrev_i32_e32 v36, 31, v20
	v_or_b32_e32 v36, 0x80000000, v36
	v_xor_b32_e32 v36, v20, v36
	v_ashrrev_i32_e32 v37, 31, v21
	v_or_b32_e32 v37, 0x80000000, v37
	v_xor_b32_e32 v37, v21, v37
	v_cmp_le_u32_e64 s[58:59], s17, v34
	v_cmp_le_u32_e64 s[60:61], s17, v35
	v_cmp_le_u32_e64 s[62:63], s17, v36
	v_cmp_le_u32_e64 s[64:65], s17, v37
	v_mov_b32_e32 v135, s26
	v_mbcnt_lo_u32_b32 v135, s58, v135
	v_mbcnt_hi_u32_b32 v135, s59, v135
	v_mbcnt_lo_u32_b32 v135, s60, v135
	v_mbcnt_hi_u32_b32 v135, s61, v135
	v_mbcnt_lo_u32_b32 v135, s62, v135
	v_mbcnt_hi_u32_b32 v135, s63, v135
	v_mbcnt_lo_u32_b32 v135, s64, v135
	v_mbcnt_hi_u32_b32 v135, s65, v135
	v_lshlrev_b32_e32 v135, 2, v135
	s_mov_b64 exec, s[58:59]
	v_add_u32_e32 v141, 0, v145
	global_store_dword v135, v141, s[40:41]
	v_add_u32_e32 v135, 4, v135
	s_mov_b64 exec, s[60:61]
	v_add_u32_e32 v142, 1, v145
	global_store_dword v135, v142, s[40:41]
	v_add_u32_e32 v135, 4, v135
	s_mov_b64 exec, s[62:63]
	v_add_u32_e32 v143, 2, v145
	global_store_dword v135, v143, s[40:41]
	v_add_u32_e32 v135, 4, v135
	s_mov_b64 exec, s[64:65]
	v_add_u32_e32 v144, 3, v145
	global_store_dword v135, v144, s[40:41]
	v_add_u32_e32 v135, 4, v135
	s_mov_b64 exec, -1
	s_bcnt1_i32_b64 s4, s[58:59]
	s_add_i32 s26, s26, s4
	s_bcnt1_i32_b64 s4, s[60:61]
	s_add_i32 s26, s26, s4
	s_bcnt1_i32_b64 s4, s[62:63]
	s_add_i32 s26, s26, s4
	s_bcnt1_i32_b64 s4, s[64:65]
	s_add_i32 s26, s26, s4
	v_ashrrev_i32_e32 v38, 31, v22
	v_or_b32_e32 v38, 0x80000000, v38
	v_xor_b32_e32 v38, v22, v38
	v_ashrrev_i32_e32 v39, 31, v23
	v_or_b32_e32 v39, 0x80000000, v39
	v_xor_b32_e32 v39, v23, v39
	v_ashrrev_i32_e32 v40, 31, v24
	v_or_b32_e32 v40, 0x80000000, v40
	v_xor_b32_e32 v40, v24, v40
	v_ashrrev_i32_e32 v41, 31, v25
	v_or_b32_e32 v41, 0x80000000, v41
	v_xor_b32_e32 v41, v25, v41
	v_cmp_le_u32_e64 s[58:59], s17, v38
	v_cmp_le_u32_e64 s[60:61], s17, v39
	v_cmp_le_u32_e64 s[62:63], s17, v40
	v_cmp_le_u32_e64 s[64:65], s17, v41
	v_mov_b32_e32 v135, s26
	v_mbcnt_lo_u32_b32 v135, s58, v135
	v_mbcnt_hi_u32_b32 v135, s59, v135
	v_mbcnt_lo_u32_b32 v135, s60, v135
	v_mbcnt_hi_u32_b32 v135, s61, v135
	v_mbcnt_lo_u32_b32 v135, s62, v135
	v_mbcnt_hi_u32_b32 v135, s63, v135
	v_mbcnt_lo_u32_b32 v135, s64, v135
	v_mbcnt_hi_u32_b32 v135, s65, v135
	v_lshlrev_b32_e32 v135, 2, v135
	s_mov_b64 exec, s[58:59]
	v_add_u32_e32 v141, 0x100, v145
	global_store_dword v135, v141, s[40:41]
	v_add_u32_e32 v135, 4, v135
	s_mov_b64 exec, s[60:61]
	v_add_u32_e32 v142, 0x101, v145
	global_store_dword v135, v142, s[40:41]
	v_add_u32_e32 v135, 4, v135
	s_mov_b64 exec, s[62:63]
	v_add_u32_e32 v143, 0x102, v145
	global_store_dword v135, v143, s[40:41]
	v_add_u32_e32 v135, 4, v135
	s_mov_b64 exec, s[64:65]
	v_add_u32_e32 v144, 0x103, v145
	global_store_dword v135, v144, s[40:41]
	v_add_u32_e32 v135, 4, v135
	s_mov_b64 exec, -1
	s_bcnt1_i32_b64 s4, s[58:59]
	s_add_i32 s26, s26, s4
	s_bcnt1_i32_b64 s4, s[60:61]
	s_add_i32 s26, s26, s4
	s_bcnt1_i32_b64 s4, s[62:63]
	s_add_i32 s26, s26, s4
	s_bcnt1_i32_b64 s4, s[64:65]
	s_add_i32 s26, s26, s4
	v_ashrrev_i32_e32 v42, 31, v26
	v_or_b32_e32 v42, 0x80000000, v42
	v_xor_b32_e32 v42, v26, v42
	v_ashrrev_i32_e32 v43, 31, v27
	v_or_b32_e32 v43, 0x80000000, v43
	v_xor_b32_e32 v43, v27, v43
	v_ashrrev_i32_e32 v44, 31, v28
	v_or_b32_e32 v44, 0x80000000, v44
	v_xor_b32_e32 v44, v28, v44
	v_ashrrev_i32_e32 v45, 31, v29
	v_or_b32_e32 v45, 0x80000000, v45
	v_xor_b32_e32 v45, v29, v45
	v_cmp_le_u32_e64 s[58:59], s17, v42
	v_cmp_le_u32_e64 s[60:61], s17, v43
	v_cmp_le_u32_e64 s[62:63], s17, v44
	v_cmp_le_u32_e64 s[64:65], s17, v45
	v_mov_b32_e32 v135, s26
	v_mbcnt_lo_u32_b32 v135, s58, v135
	v_mbcnt_hi_u32_b32 v135, s59, v135
	v_mbcnt_lo_u32_b32 v135, s60, v135
	v_mbcnt_hi_u32_b32 v135, s61, v135
	v_mbcnt_lo_u32_b32 v135, s62, v135
	v_mbcnt_hi_u32_b32 v135, s63, v135
	v_mbcnt_lo_u32_b32 v135, s64, v135
	v_mbcnt_hi_u32_b32 v135, s65, v135
	v_lshlrev_b32_e32 v135, 2, v135
	s_mov_b64 exec, s[58:59]
	v_add_u32_e32 v141, 0x200, v145
	global_store_dword v135, v141, s[40:41]
	v_add_u32_e32 v135, 4, v135
	s_mov_b64 exec, s[60:61]
	v_add_u32_e32 v142, 0x201, v145
	global_store_dword v135, v142, s[40:41]
	v_add_u32_e32 v135, 4, v135
	s_mov_b64 exec, s[62:63]
	v_add_u32_e32 v143, 0x202, v145
	global_store_dword v135, v143, s[40:41]
	v_add_u32_e32 v135, 4, v135
	s_mov_b64 exec, s[64:65]
	v_add_u32_e32 v144, 0x203, v145
	global_store_dword v135, v144, s[40:41]
	v_add_u32_e32 v135, 4, v135
	s_mov_b64 exec, -1
	s_bcnt1_i32_b64 s4, s[58:59]
	s_add_i32 s26, s26, s4
	s_bcnt1_i32_b64 s4, s[60:61]
	s_add_i32 s26, s26, s4
	s_bcnt1_i32_b64 s4, s[62:63]
	s_add_i32 s26, s26, s4
	s_bcnt1_i32_b64 s4, s[64:65]
	s_add_i32 s26, s26, s4
	v_ashrrev_i32_e32 v46, 31, v30
	v_or_b32_e32 v46, 0x80000000, v46
	v_xor_b32_e32 v46, v30, v46
	v_ashrrev_i32_e32 v47, 31, v31
	v_or_b32_e32 v47, 0x80000000, v47
	v_xor_b32_e32 v47, v31, v47
	v_ashrrev_i32_e32 v48, 31, v32
	v_or_b32_e32 v48, 0x80000000, v48
	v_xor_b32_e32 v48, v32, v48
	v_ashrrev_i32_e32 v49, 31, v33
	v_or_b32_e32 v49, 0x80000000, v49
	v_xor_b32_e32 v49, v33, v49
	v_cmp_le_u32_e64 s[58:59], s17, v46
	v_cmp_le_u32_e64 s[60:61], s17, v47
	v_cmp_le_u32_e64 s[62:63], s17, v48
	v_cmp_le_u32_e64 s[64:65], s17, v49
	v_mov_b32_e32 v135, s26
	v_mbcnt_lo_u32_b32 v135, s58, v135
	v_mbcnt_hi_u32_b32 v135, s59, v135
	v_mbcnt_lo_u32_b32 v135, s60, v135
	v_mbcnt_hi_u32_b32 v135, s61, v135
	v_mbcnt_lo_u32_b32 v135, s62, v135
	v_mbcnt_hi_u32_b32 v135, s63, v135
	v_mbcnt_lo_u32_b32 v135, s64, v135
	v_mbcnt_hi_u32_b32 v135, s65, v135
	v_lshlrev_b32_e32 v135, 2, v135
	s_mov_b64 exec, s[58:59]
	v_add_u32_e32 v141, 0x300, v145
	global_store_dword v135, v141, s[40:41]
	v_add_u32_e32 v135, 4, v135
	s_mov_b64 exec, s[60:61]
	v_add_u32_e32 v142, 0x301, v145
	global_store_dword v135, v142, s[40:41]
	v_add_u32_e32 v135, 4, v135
	s_mov_b64 exec, s[62:63]
	v_add_u32_e32 v143, 0x302, v145
	global_store_dword v135, v143, s[40:41]
	v_add_u32_e32 v135, 4, v135
	s_mov_b64 exec, s[64:65]
	v_add_u32_e32 v144, 0x303, v145
	global_store_dword v135, v144, s[40:41]
	v_add_u32_e32 v135, 4, v135
	s_mov_b64 exec, -1
	s_bcnt1_i32_b64 s4, s[58:59]
	s_add_i32 s26, s26, s4
	s_bcnt1_i32_b64 s4, s[60:61]
	s_add_i32 s26, s26, s4
	s_bcnt1_i32_b64 s4, s[62:63]
	s_add_i32 s26, s26, s4
	s_bcnt1_i32_b64 s4, s[64:65]
	s_add_i32 s26, s26, s4
	s_mov_b32 s16, s36
	s_cmp_lt_i32 s16, s2
	s_cbranch_scc0 .Lsel_fs_done
	s_waitcnt vmcnt(16)
	s_branch .Lsel_fs_loop
.Lsel_fs_tail:
	s_sub_i32 s37, s2, s16
	v_sub_u32_e32 v134, s37, v56
	v_add_u32_e32 v145, s16, v56
	v_ashrrev_i32_e32 v34, 31, v18
	v_or_b32_e32 v34, 0x80000000, v34
	v_xor_b32_e32 v34, v18, v34
	v_ashrrev_i32_e32 v35, 31, v19
	v_or_b32_e32 v35, 0x80000000, v35
	v_xor_b32_e32 v35, v19, v35
	v_ashrrev_i32_e32 v36, 31, v20
	v_or_b32_e32 v36, 0x80000000, v36
	v_xor_b32_e32 v36, v20, v36
	v_ashrrev_i32_e32 v37, 31, v21
	v_or_b32_e32 v37, 0x80000000, v37
	v_xor_b32_e32 v37, v21, v37
	v_cmpx_lt_i32_e32 vcc, 0, v134
	v_cmp_le_u32_e64 s[58:59], s17, v34
	v_cmpx_lt_i32_e32 vcc, 1, v134
	v_cmp_le_u32_e64 s[60:61], s17, v35
	v_cmpx_lt_i32_e32 vcc, 2, v134
	v_cmp_le_u32_e64 s[62:63], s17, v36
	v_cmpx_lt_i32_e32 vcc, 3, v134
	v_cmp_le_u32_e64 s[64:65], s17, v37
	s_mov_b64 exec, -1
	v_mov_b32_e32 v135, s26
	v_mbcnt_lo_u32_b32 v135, s58, v135
	v_mbcnt_hi_u32_b32 v135, s59, v135
	v_mbcnt_lo_u32_b32 v135, s60, v135
	v_mbcnt_hi_u32_b32 v135, s61, v135
	v_mbcnt_lo_u32_b32 v135, s62, v135
	v_mbcnt_hi_u32_b32 v135, s63, v135
	v_mbcnt_lo_u32_b32 v135, s64, v135
	v_mbcnt_hi_u32_b32 v135, s65, v135
	v_lshlrev_b32_e32 v135, 2, v135
	s_mov_b64 exec, s[58:59]
	v_add_u32_e32 v141, 0, v145
	global_store_dword v135, v141, s[40:41]
	v_add_u32_e32 v135, 4, v135
	s_mov_b64 exec, s[60:61]
	v_add_u32_e32 v142, 1, v145
	global_store_dword v135, v142, s[40:41]
	v_add_u32_e32 v135, 4, v135
	s_mov_b64 exec, s[62:63]
	v_add_u32_e32 v143, 2, v145
	global_store_dword v135, v143, s[40:41]
	v_add_u32_e32 v135, 4, v135
	s_mov_b64 exec, s[64:65]
	v_add_u32_e32 v144, 3, v145
	global_store_dword v135, v144, s[40:41]
	v_add_u32_e32 v135, 4, v135
	s_mov_b64 exec, -1
	s_bcnt1_i32_b64 s4, s[58:59]
	s_add_i32 s26, s26, s4
	s_bcnt1_i32_b64 s4, s[60:61]
	s_add_i32 s26, s26, s4
	s_bcnt1_i32_b64 s4, s[62:63]
	s_add_i32 s26, s26, s4
	s_bcnt1_i32_b64 s4, s[64:65]
	s_add_i32 s26, s26, s4
	v_ashrrev_i32_e32 v38, 31, v22
	v_or_b32_e32 v38, 0x80000000, v38
	v_xor_b32_e32 v38, v22, v38
	v_ashrrev_i32_e32 v39, 31, v23
	v_or_b32_e32 v39, 0x80000000, v39
	v_xor_b32_e32 v39, v23, v39
	v_ashrrev_i32_e32 v40, 31, v24
	v_or_b32_e32 v40, 0x80000000, v40
	v_xor_b32_e32 v40, v24, v40
	v_ashrrev_i32_e32 v41, 31, v25
	v_or_b32_e32 v41, 0x80000000, v41
	v_xor_b32_e32 v41, v25, v41
	v_cmpx_lt_i32_e32 vcc, 0x100, v134
	v_cmp_le_u32_e64 s[58:59], s17, v38
	v_cmpx_lt_i32_e32 vcc, 0x101, v134
	v_cmp_le_u32_e64 s[60:61], s17, v39
	v_cmpx_lt_i32_e32 vcc, 0x102, v134
	v_cmp_le_u32_e64 s[62:63], s17, v40
	v_cmpx_lt_i32_e32 vcc, 0x103, v134
	v_cmp_le_u32_e64 s[64:65], s17, v41
	s_mov_b64 exec, -1
	v_mov_b32_e32 v135, s26
	v_mbcnt_lo_u32_b32 v135, s58, v135
	v_mbcnt_hi_u32_b32 v135, s59, v135
	v_mbcnt_lo_u32_b32 v135, s60, v135
	v_mbcnt_hi_u32_b32 v135, s61, v135
	v_mbcnt_lo_u32_b32 v135, s62, v135
	v_mbcnt_hi_u32_b32 v135, s63, v135
	v_mbcnt_lo_u32_b32 v135, s64, v135
	v_mbcnt_hi_u32_b32 v135, s65, v135
	v_lshlrev_b32_e32 v135, 2, v135
	s_mov_b64 exec, s[58:59]
	v_add_u32_e32 v141, 0x100, v145
	global_store_dword v135, v141, s[40:41]
	v_add_u32_e32 v135, 4, v135
	s_mov_b64 exec, s[60:61]
	v_add_u32_e32 v142, 0x101, v145
	global_store_dword v135, v142, s[40:41]
	v_add_u32_e32 v135, 4, v135
	s_mov_b64 exec, s[62:63]
	v_add_u32_e32 v143, 0x102, v145
	global_store_dword v135, v143, s[40:41]
	v_add_u32_e32 v135, 4, v135
	s_mov_b64 exec, s[64:65]
	v_add_u32_e32 v144, 0x103, v145
	global_store_dword v135, v144, s[40:41]
	v_add_u32_e32 v135, 4, v135
	s_mov_b64 exec, -1
	s_bcnt1_i32_b64 s4, s[58:59]
	s_add_i32 s26, s26, s4
	s_bcnt1_i32_b64 s4, s[60:61]
	s_add_i32 s26, s26, s4
	s_bcnt1_i32_b64 s4, s[62:63]
	s_add_i32 s26, s26, s4
	s_bcnt1_i32_b64 s4, s[64:65]
	s_add_i32 s26, s26, s4
	v_ashrrev_i32_e32 v42, 31, v26
	v_or_b32_e32 v42, 0x80000000, v42
	v_xor_b32_e32 v42, v26, v42
	v_ashrrev_i32_e32 v43, 31, v27
	v_or_b32_e32 v43, 0x80000000, v43
	v_xor_b32_e32 v43, v27, v43
	v_ashrrev_i32_e32 v44, 31, v28
	v_or_b32_e32 v44, 0x80000000, v44
	v_xor_b32_e32 v44, v28, v44
	v_ashrrev_i32_e32 v45, 31, v29
	v_or_b32_e32 v45, 0x80000000, v45
	v_xor_b32_e32 v45, v29, v45
	v_cmpx_lt_i32_e32 vcc, 0x200, v134
	v_cmp_le_u32_e64 s[58:59], s17, v42
	v_cmpx_lt_i32_e32 vcc, 0x201, v134
	v_cmp_le_u32_e64 s[60:61], s17, v43
	v_cmpx_lt_i32_e32 vcc, 0x202, v134
	v_cmp_le_u32_e64 s[62:63], s17, v44
	v_cmpx_lt_i32_e32 vcc, 0x203, v134
	v_cmp_le_u32_e64 s[64:65], s17, v45
	s_mov_b64 exec, -1
	v_mov_b32_e32 v135, s26
	v_mbcnt_lo_u32_b32 v135, s58, v135
	v_mbcnt_hi_u32_b32 v135, s59, v135
	v_mbcnt_lo_u32_b32 v135, s60, v135
	v_mbcnt_hi_u32_b32 v135, s61, v135
	v_mbcnt_lo_u32_b32 v135, s62, v135
	v_mbcnt_hi_u32_b32 v135, s63, v135
	v_mbcnt_lo_u32_b32 v135, s64, v135
	v_mbcnt_hi_u32_b32 v135, s65, v135
	v_lshlrev_b32_e32 v135, 2, v135
	s_mov_b64 exec, s[58:59]
	v_add_u32_e32 v141, 0x200, v145
	global_store_dword v135, v141, s[40:41]
	v_add_u32_e32 v135, 4, v135
	s_mov_b64 exec, s[60:61]
	v_add_u32_e32 v142, 0x201, v145
	global_store_dword v135, v142, s[40:41]
	v_add_u32_e32 v135, 4, v135
	s_mov_b64 exec, s[62:63]
	v_add_u32_e32 v143, 0x202, v145
	global_store_dword v135, v143, s[40:41]
	v_add_u32_e32 v135, 4, v135
	s_mov_b64 exec, s[64:65]
	v_add_u32_e32 v144, 0x203, v145
	global_store_dword v135, v144, s[40:41]
	v_add_u32_e32 v135, 4, v135
	s_mov_b64 exec, -1
	s_bcnt1_i32_b64 s4, s[58:59]
	s_add_i32 s26, s26, s4
	s_bcnt1_i32_b64 s4, s[60:61]
	s_add_i32 s26, s26, s4
	s_bcnt1_i32_b64 s4, s[62:63]
	s_add_i32 s26, s26, s4
	s_bcnt1_i32_b64 s4, s[64:65]
	s_add_i32 s26, s26, s4
	v_ashrrev_i32_e32 v46, 31, v30
	v_or_b32_e32 v46, 0x80000000, v46
	v_xor_b32_e32 v46, v30, v46
	v_ashrrev_i32_e32 v47, 31, v31
	v_or_b32_e32 v47, 0x80000000, v47
	v_xor_b32_e32 v47, v31, v47
	v_ashrrev_i32_e32 v48, 31, v32
	v_or_b32_e32 v48, 0x80000000, v48
	v_xor_b32_e32 v48, v32, v48
	v_ashrrev_i32_e32 v49, 31, v33
	v_or_b32_e32 v49, 0x80000000, v49
	v_xor_b32_e32 v49, v33, v49
	v_cmpx_lt_i32_e32 vcc, 0x300, v134
	v_cmp_le_u32_e64 s[58:59], s17, v46
	v_cmpx_lt_i32_e32 vcc, 0x301, v134
	v_cmp_le_u32_e64 s[60:61], s17, v47
	v_cmpx_lt_i32_e32 vcc, 0x302, v134
	v_cmp_le_u32_e64 s[62:63], s17, v48
	v_cmpx_lt_i32_e32 vcc, 0x303, v134
	v_cmp_le_u32_e64 s[64:65], s17, v49
	s_mov_b64 exec, -1
	v_mov_b32_e32 v135, s26
	v_mbcnt_lo_u32_b32 v135, s58, v135
	v_mbcnt_hi_u32_b32 v135, s59, v135
	v_mbcnt_lo_u32_b32 v135, s60, v135
	v_mbcnt_hi_u32_b32 v135, s61, v135
	v_mbcnt_lo_u32_b32 v135, s62, v135
	v_mbcnt_hi_u32_b32 v135, s63, v135
	v_mbcnt_lo_u32_b32 v135, s64, v135
	v_mbcnt_hi_u32_b32 v135, s65, v135
	v_lshlrev_b32_e32 v135, 2, v135
	s_mov_b64 exec, s[58:59]
	v_add_u32_e32 v141, 0x300, v145
	global_store_dword v135, v141, s[40:41]
	v_add_u32_e32 v135, 4, v135
	s_mov_b64 exec, s[60:61]
	v_add_u32_e32 v142, 0x301, v145
	global_store_dword v135, v142, s[40:41]
	v_add_u32_e32 v135, 4, v135
	s_mov_b64 exec, s[62:63]
	v_add_u32_e32 v143, 0x302, v145
	global_store_dword v135, v143, s[40:41]
	v_add_u32_e32 v135, 4, v135
	s_mov_b64 exec, s[64:65]
	v_add_u32_e32 v144, 0x303, v145
	global_store_dword v135, v144, s[40:41]
	v_add_u32_e32 v135, 4, v135
	s_mov_b64 exec, -1
	s_bcnt1_i32_b64 s4, s[58:59]
	s_add_i32 s26, s26, s4
	s_bcnt1_i32_b64 s4, s[60:61]
	s_add_i32 s26, s26, s4
	s_bcnt1_i32_b64 s4, s[62:63]
	s_add_i32 s26, s26, s4
	s_bcnt1_i32_b64 s4, s[64:65]
	s_add_i32 s26, s26, s4

	.amdhsa_kernel _Z10hybrid_fwd4Args
		.amdhsa_group_segment_fixed_size 0
		.amdhsa_private_segment_fixed_size 0
		.amdhsa_kernarg_size 464
		.amdhsa_user_sgpr_count 2
		.amdhsa_user_sgpr_dispatch_ptr 0
		.amdhsa_user_sgpr_queue_ptr 0
		.amdhsa_user_sgpr_kernarg_segment_ptr 1
		.amdhsa_user_sgpr_dispatch_id 0
		.amdhsa_user_sgpr_kernarg_preload_length 0
		.amdhsa_user_sgpr_kernarg_preload_offset 0
		.amdhsa_user_sgpr_private_segment_size 0
		.amdhsa_uses_dynamic_stack 0
		.amdhsa_enable_private_segment 0
		.amdhsa_system_sgpr_workgroup_id_x 1
		.amdhsa_system_sgpr_workgroup_id_y 0
		.amdhsa_system_sgpr_workgroup_id_z 0
		.amdhsa_system_sgpr_workgroup_info 0
		.amdhsa_system_vgpr_workitem_id 0
		.amdhsa_next_free_vgpr 256
		.amdhsa_next_free_sgpr 102
		.amdhsa_accum_offset 256
		.amdhsa_reserve_vcc 1
		.amdhsa_float_round_mode_32 0
		.amdhsa_float_round_mode_16_64 0
		.amdhsa_float_denorm_mode_32 3
		.amdhsa_float_denorm_mode_16_64 3
		.amdhsa_dx10_clamp 1
		.amdhsa_ieee_mode 1
		.amdhsa_fp16_overflow 0
		.amdhsa_tg_split 0
		.amdhsa_exception_fp_ieee_invalid_op 0
		.amdhsa_exception_fp_denorm_src 0
		.amdhsa_exception_fp_ieee_div_zero 0
		.amdhsa_exception_fp_ieee_overflow 0
		.amdhsa_exception_fp_ieee_underflow 0
		.amdhsa_exception_fp_ieee_inexact 0
		.amdhsa_exception_int_div_zero 0
	.end_amdhsa_kernel

amdhsa.kernels:
  - .agpr_count:     0
    .args:
      - .offset:         0
        .size:           208
        .value_kind:     by_value
      - .offset:         208
        .size:           4
        .value_kind:     hidden_block_count_x
      - .offset:         212
        .size:           4
        .value_kind:     hidden_block_count_y
      - .offset:         216
        .size:           4
        .value_kind:     hidden_block_count_z
      - .offset:         220
        .size:           2
        .value_kind:     hidden_group_size_x
      - .offset:         222
        .size:           2
        .value_kind:     hidden_group_size_y
      - .offset:         224
        .size:           2
        .value_kind:     hidden_group_size_z
      - .offset:         226
        .size:           2
        .value_kind:     hidden_remainder_x
      - .offset:         228
        .size:           2
        .value_kind:     hidden_remainder_y
      - .offset:         230
        .size:           2
        .value_kind:     hidden_remainder_z
      - .offset:         248
        .size:           8
        .value_kind:     hidden_global_offset_x
      - .offset:         256
        .size:           8
        .value_kind:     hidden_global_offset_y
      - .offset:         264
        .size:           8
        .value_kind:     hidden_global_offset_z
      - .offset:         272
        .size:           2
        .value_kind:     hidden_grid_dims
      - .offset:         328
        .size:           4
        .value_kind:     hidden_dynamic_lds_size
    .group_segment_fixed_size: 0
    .kernarg_segment_align: 8
    .kernarg_segment_size: 464
    .language:       OpenCL C
    .language_version:
      - 2
      - 0
    .max_flat_workgroup_size: 512
    .name:           _Z10hybrid_fwd4Args
    .private_segment_fixed_size: 0
    .sgpr_count:     108
    .sgpr_spill_count: 78
    .symbol:         _Z10hybrid_fwd4Args.kd
    .uniform_work_group_size: 1
    .uses_dynamic_stack: false
    .vgpr_count:     256
    .vgpr_spill_count: 0
    .wavefront_size: 64
